# P0 silu(c) loop: 16 dependent loads issued together (one round trip instead of sixteen)
# speedup vs baseline: 1.0083x; 1.0083x over previous
.LBB0_15:
	s_lshr_b32 s86, s87, 6
	s_cmp_lt_i32 s28, 1
	s_load_dwordx16 s[12:27], s[0:1], 0x40
	s_cselect_b64 s[62:63], -1, 0
	s_cmp_gt_i32 s28, 0
	s_cselect_b64 s[0:1], -1, 0
	s_cmp_lt_i32 s29, 1
	s_cselect_b64 s[4:5], -1, 0
	v_writelane_b32 v255, s86, 4
	s_or_b64 s[0:1], s[0:1], s[4:5]
	v_writelane_b32 v255, s87, 5
	v_and_b32_e32 v254, 63, v0
	s_and_b64 vcc, exec, s[0:1]
	v_writelane_b32 v255, s88, 6
	s_cbranch_vccnz .LBB0_57
	v_lshlrev_b32_e32 v2, 2, v0
	v_add_u32_e32 v5, 0x18000, v2
	v_add_u32_e32 v3, 0x1000, v2
	v_add_u32_e32 v4, 0x2000, v2
	v_add_u32_e32 v22, 0x3000, v2
	global_load_dword v6, v2, s[38:39]
	global_load_dword v7, v2, s[38:39] offset:2048
	global_load_dword v8, v3, s[38:39]
	global_load_dword v9, v3, s[38:39] offset:2048
	global_load_dword v10, v4, s[38:39]
	global_load_dword v11, v4, s[38:39] offset:2048
	global_load_dword v12, v22, s[38:39]
	global_load_dword v13, v22, s[38:39] offset:2048
	v_add_u32_e32 v3, 0x4000, v2
	v_add_u32_e32 v4, 0x5000, v2
	v_add_u32_e32 v22, 0x6000, v2
	v_add_u32_e32 v23, 0x7000, v2
	global_load_dword v14, v3, s[38:39]
	global_load_dword v15, v3, s[38:39] offset:2048
	global_load_dword v16, v4, s[38:39]
	global_load_dword v17, v4, s[38:39] offset:2048
	global_load_dword v18, v22, s[38:39]
	global_load_dword v19, v22, s[38:39] offset:2048
	global_load_dword v20, v23, s[38:39]
	global_load_dword v21, v23, s[38:39] offset:2048
	s_waitcnt vmcnt(12)
	v_mul_f32_e32 v3, 0xbfb8aa3b, v6
	v_mul_f32_e32 v4, 0xbfb8aa3b, v7
	v_mul_f32_e32 v22, 0xbfb8aa3b, v8
	v_mul_f32_e32 v23, 0xbfb8aa3b, v9
	v_exp_f32_e32 v3, v3
	v_exp_f32_e32 v4, v4
	v_exp_f32_e32 v22, v22
	v_exp_f32_e32 v23, v23
	s_nop 0
	v_add_f32_e32 v3, 1.0, v3
	v_add_f32_e32 v4, 1.0, v4
	v_add_f32_e32 v22, 1.0, v22
	v_add_f32_e32 v23, 1.0, v23
	v_rcp_f32_e32 v3, v3
	v_rcp_f32_e32 v4, v4
	v_rcp_f32_e32 v22, v22
	v_rcp_f32_e32 v23, v23
	s_nop 0
	v_mul_f32_e32 v6, v6, v3
	v_mul_f32_e32 v7, v7, v4
	v_mul_f32_e32 v8, v8, v22
	v_mul_f32_e32 v9, v9, v23
	ds_write_b32 v5, v6 offset:0
	ds_write_b32 v5, v7 offset:2048
	ds_write_b32 v5, v8 offset:4096
	ds_write_b32 v5, v9 offset:6144
	s_waitcnt vmcnt(8)
	v_mul_f32_e32 v3, 0xbfb8aa3b, v10
	v_mul_f32_e32 v4, 0xbfb8aa3b, v11
	v_mul_f32_e32 v22, 0xbfb8aa3b, v12
	v_mul_f32_e32 v23, 0xbfb8aa3b, v13
	v_exp_f32_e32 v3, v3
	v_exp_f32_e32 v4, v4
	v_exp_f32_e32 v22, v22
	v_exp_f32_e32 v23, v23
	s_nop 0
	v_add_f32_e32 v3, 1.0, v3
	v_add_f32_e32 v4, 1.0, v4
	v_add_f32_e32 v22, 1.0, v22
	v_add_f32_e32 v23, 1.0, v23
	v_rcp_f32_e32 v3, v3
	v_rcp_f32_e32 v4, v4
	v_rcp_f32_e32 v22, v22
	v_rcp_f32_e32 v23, v23
	s_nop 0
	v_mul_f32_e32 v10, v10, v3
	v_mul_f32_e32 v11, v11, v4
	v_mul_f32_e32 v12, v12, v22
	v_mul_f32_e32 v13, v13, v23
	ds_write_b32 v5, v10 offset:8192
	ds_write_b32 v5, v11 offset:10240
	ds_write_b32 v5, v12 offset:12288
	ds_write_b32 v5, v13 offset:14336
	s_waitcnt vmcnt(4)
	v_mul_f32_e32 v3, 0xbfb8aa3b, v14
	v_mul_f32_e32 v4, 0xbfb8aa3b, v15
	v_mul_f32_e32 v22, 0xbfb8aa3b, v16
	v_mul_f32_e32 v23, 0xbfb8aa3b, v17
	v_exp_f32_e32 v3, v3
	v_exp_f32_e32 v4, v4
	v_exp_f32_e32 v22, v22
	v_exp_f32_e32 v23, v23
	s_nop 0
	v_add_f32_e32 v3, 1.0, v3
	v_add_f32_e32 v4, 1.0, v4
	v_add_f32_e32 v22, 1.0, v22
	v_add_f32_e32 v23, 1.0, v23
	v_rcp_f32_e32 v3, v3
	v_rcp_f32_e32 v4, v4
	v_rcp_f32_e32 v22, v22
	v_rcp_f32_e32 v23, v23
	s_nop 0
	v_mul_f32_e32 v14, v14, v3
	v_mul_f32_e32 v15, v15, v4
	v_mul_f32_e32 v16, v16, v22
	v_mul_f32_e32 v17, v17, v23
	ds_write_b32 v5, v14 offset:16384
	ds_write_b32 v5, v15 offset:18432
	ds_write_b32 v5, v16 offset:20480
	ds_write_b32 v5, v17 offset:22528
	s_waitcnt vmcnt(0)
	v_mul_f32_e32 v3, 0xbfb8aa3b, v18
	v_mul_f32_e32 v4, 0xbfb8aa3b, v19
	v_mul_f32_e32 v22, 0xbfb8aa3b, v20
	v_mul_f32_e32 v23, 0xbfb8aa3b, v21
	v_exp_f32_e32 v3, v3
	v_exp_f32_e32 v4, v4
	v_exp_f32_e32 v22, v22
	v_exp_f32_e32 v23, v23
	s_nop 0
	v_add_f32_e32 v3, 1.0, v3
	v_add_f32_e32 v4, 1.0, v4
	v_add_f32_e32 v22, 1.0, v22
	v_add_f32_e32 v23, 1.0, v23
	v_rcp_f32_e32 v3, v3
	v_rcp_f32_e32 v4, v4
	v_rcp_f32_e32 v22, v22
	v_rcp_f32_e32 v23, v23
	s_nop 0
	v_mul_f32_e32 v18, v18, v3
	v_mul_f32_e32 v19, v19, v4
	v_mul_f32_e32 v20, v20, v22
	v_mul_f32_e32 v21, v21, v23
	ds_write_b32 v5, v18 offset:24576
	ds_write_b32 v5, v19 offset:26624
	ds_write_b32 v5, v20 offset:28672
	ds_write_b32 v5, v21 offset:30720
	s_cmpk_gt_u32 s87, 0xbf
	s_mov_b64 s[0:1], -1
	s_waitcnt lgkmcnt(0)
	s_barrier
	s_cbranch_scc0 .LBB0_27
	s_add_i32 s0, s86, -3
	s_mul_i32 s1, s76, 5
	s_add_i32 s91, s1, s0
	s_cmpk_gt_i32 s91, 0x19ff
	s_cbranch_scc1 .LBB0_26
	s_mul_hi_i32 s1, s91, 0x4ec4ec4f
	s_lshr_b32 s3, s1, 31
	s_ashr_i32 s1, s1, 6
	s_add_i32 s1, s1, s3
	s_mulk_i32 s0, 0x4200
	s_mul_i32 s3, s1, 0xd0
	s_add_i32 s0, s0, 0
	s_sub_i32 s3, s91, s3
	s_lshl_b32 s4, s1, 6
	s_mul_i32 s1, s1, 0x340000
	s_mul_hi_i32 s4, s4, 0xd000
	s_add_u32 s1, s46, s1
	s_addc_u32 s6, s47, s4
	s_lshl_b32 s4, s3, 6
	s_ashr_i32 s5, s4, 31
	s_lshl_b64 s[4:5], s[4:5], 2
	v_lshlrev_b32_e32 v2, 1, v0
	s_add_u32 s4, s1, s4
	v_and_b32_e32 v4, 62, v2
	v_lshrrev_b32_e32 v5, 5, v254
	s_addc_u32 s5, s6, s5
	v_mov_b32_e32 v3, 0
	v_lshlrev_b32_e32 v2, 2, v4
	v_mul_u32_u24_e32 v8, 0x3400, v5
	v_lshl_add_u64 v[6:7], s[4:5], 0, v[2:3]
	v_lshlrev_b32_e32 v10, 2, v8
	v_mov_b32_e32 v11, v3
	v_lshl_add_u64 v[6:7], v[6:7], 0, v[10:11]
	s_mov_b32 s3, 0x1a000
	v_add_co_u32_e32 v10, vcc, s3, v6
	s_mov_b32 s6, 0x34000
	s_nop 0
	v_addc_co_u32_e32 v11, vcc, 0, v7, vcc
	v_add_co_u32_e32 v12, vcc, s6, v6
	s_mov_b32 s7, 0x4e000
	s_nop 0
	v_addc_co_u32_e32 v13, vcc, 0, v7, vcc
	v_add_co_u32_e32 v14, vcc, s7, v6
	s_mov_b32 s8, 0x68000
	s_nop 0
	v_addc_co_u32_e32 v15, vcc, 0, v7, vcc
	global_load_dwordx2 v[84:85], v[6:7], off
	global_load_dwordx2 v[76:77], v[10:11], off
	global_load_dwordx2 v[74:75], v[12:13], off
	global_load_dwordx2 v[72:73], v[14:15], off
	v_add_co_u32_e32 v10, vcc, s8, v6
	s_mov_b32 s9, 0x82000
	s_nop 0
	v_addc_co_u32_e32 v11, vcc, 0, v7, vcc
	v_add_co_u32_e32 v12, vcc, s9, v6
	s_mov_b32 s34, 0x9c000
	s_nop 0
	v_addc_co_u32_e32 v13, vcc, 0, v7, vcc
	v_add_co_u32_e32 v14, vcc, s34, v6
	s_mov_b32 s35, 0xb6000
	s_nop 0
	v_addc_co_u32_e32 v15, vcc, 0, v7, vcc
	v_add_co_u32_e32 v16, vcc, s35, v6
	s_mov_b32 s38, 0xd0000
	s_nop 0
	v_addc_co_u32_e32 v17, vcc, 0, v7, vcc
	global_load_dwordx2 v[94:95], v[10:11], off
	global_load_dwordx2 v[92:93], v[12:13], off
	global_load_dwordx2 v[90:91], v[14:15], off
	global_load_dwordx2 v[88:89], v[16:17], off
	v_add_co_u32_e32 v10, vcc, s38, v6
	s_mov_b32 s39, 0xea000
	s_nop 0
	v_addc_co_u32_e32 v11, vcc, 0, v7, vcc
	v_add_co_u32_e32 v12, vcc, s39, v6
	s_mov_b32 s60, 0x104000
	s_nop 0
	v_addc_co_u32_e32 v13, vcc, 0, v7, vcc
	v_add_co_u32_e32 v14, vcc, s60, v6
	s_mov_b32 s61, 0x11e000
	s_nop 0
	v_addc_co_u32_e32 v15, vcc, 0, v7, vcc
	v_add_co_u32_e32 v16, vcc, s61, v6
	s_mov_b32 s64, 0x138000
	s_nop 0
	v_addc_co_u32_e32 v17, vcc, 0, v7, vcc
	global_load_dwordx2 v[110:111], v[10:11], off
	global_load_dwordx2 v[108:109], v[12:13], off
	global_load_dwordx2 v[106:107], v[14:15], off
	global_load_dwordx2 v[104:105], v[16:17], off
	v_add_co_u32_e32 v10, vcc, s64, v6
	s_mov_b32 s65, 0x152000
	s_nop 0
	v_addc_co_u32_e32 v11, vcc, 0, v7, vcc
	v_add_co_u32_e32 v12, vcc, s65, v6
	s_mov_b32 s66, 0x16c000
	s_nop 0
	v_addc_co_u32_e32 v13, vcc, 0, v7, vcc
	v_add_co_u32_e32 v14, vcc, s66, v6
	s_mov_b32 s67, 0x186000
	s_nop 0
	v_addc_co_u32_e32 v15, vcc, 0, v7, vcc
	v_add_co_u32_e32 v16, vcc, s67, v6
	s_mov_b32 s68, 0x1a0000
	s_nop 0
	v_addc_co_u32_e32 v17, vcc, 0, v7, vcc
	global_load_dwordx2 v[118:119], v[10:11], off
	global_load_dwordx2 v[116:117], v[12:13], off
	global_load_dwordx2 v[114:115], v[14:15], off
	global_load_dwordx2 v[112:113], v[16:17], off
	v_add_co_u32_e32 v10, vcc, s68, v6
	s_mov_b32 s69, 0x1ba000
	s_nop 0
	v_addc_co_u32_e32 v11, vcc, 0, v7, vcc
	v_add_co_u32_e32 v12, vcc, s69, v6
	s_mov_b32 s70, 0x1d4000
	s_nop 0
	v_addc_co_u32_e32 v13, vcc, 0, v7, vcc
	v_add_co_u32_e32 v14, vcc, s70, v6
	s_mov_b32 s71, 0x1ee000
	s_nop 0
	v_addc_co_u32_e32 v15, vcc, 0, v7, vcc
	v_add_co_u32_e32 v16, vcc, s71, v6
	s_mov_b32 s77, 0x208000
	s_nop 0
	v_addc_co_u32_e32 v17, vcc, 0, v7, vcc
	global_load_dwordx2 v[126:127], v[10:11], off
	global_load_dwordx2 v[124:125], v[12:13], off
	global_load_dwordx2 v[122:123], v[14:15], off
	global_load_dwordx2 v[120:121], v[16:17], off
	v_add_co_u32_e32 v10, vcc, s77, v6
	s_mov_b32 s78, 0x222000
	s_nop 0
	v_addc_co_u32_e32 v11, vcc, 0, v7, vcc
	v_add_co_u32_e32 v12, vcc, s78, v6
	s_mov_b32 s79, 0x23c000
	s_nop 0
	v_addc_co_u32_e32 v13, vcc, 0, v7, vcc
	v_add_co_u32_e32 v14, vcc, s79, v6
	s_mov_b32 s80, 0x256000
	s_nop 0
	v_addc_co_u32_e32 v15, vcc, 0, v7, vcc
	v_add_co_u32_e32 v16, vcc, s80, v6
	s_mov_b32 s81, 0x270000
	s_nop 0
	v_addc_co_u32_e32 v17, vcc, 0, v7, vcc
	global_load_dwordx2 v[134:135], v[10:11], off
	global_load_dwordx2 v[132:133], v[12:13], off
	global_load_dwordx2 v[130:131], v[14:15], off
	global_load_dwordx2 v[128:129], v[16:17], off
	v_add_co_u32_e32 v10, vcc, s81, v6
	s_mov_b32 s82, 0x28a000
	s_nop 0
	v_addc_co_u32_e32 v11, vcc, 0, v7, vcc
	v_add_co_u32_e32 v12, vcc, s82, v6
	s_mov_b32 s83, 0x2a4000
	s_nop 0
	v_addc_co_u32_e32 v13, vcc, 0, v7, vcc
	v_add_co_u32_e32 v14, vcc, s83, v6
	s_mov_b32 s84, 0x2be000
	s_nop 0
	v_addc_co_u32_e32 v15, vcc, 0, v7, vcc
	v_add_co_u32_e32 v16, vcc, s84, v6
	s_mov_b32 s1, 0x2d8000
	s_nop 0
	v_addc_co_u32_e32 v17, vcc, 0, v7, vcc
	global_load_dwordx2 v[142:143], v[10:11], off
	global_load_dwordx2 v[140:141], v[12:13], off
	global_load_dwordx2 v[138:139], v[14:15], off
	global_load_dwordx2 v[136:137], v[16:17], off
	v_add_co_u32_e32 v10, vcc, s1, v6
	s_mov_b32 s1, 0x2f2000
	s_nop 0
	v_addc_co_u32_e32 v11, vcc, 0, v7, vcc
	v_add_co_u32_e32 v12, vcc, s1, v6
	s_mov_b32 s1, 0x30c000
	s_nop 0
	v_addc_co_u32_e32 v13, vcc, 0, v7, vcc
	v_add_co_u32_e32 v14, vcc, s1, v6
	s_mov_b32 s1, 0x326000
	s_nop 0
	v_addc_co_u32_e32 v15, vcc, 0, v7, vcc
	v_add_co_u32_e32 v6, vcc, s1, v6
	s_mul_i32 s85, s33, 5
	s_nop 0
	v_addc_co_u32_e32 v7, vcc, 0, v7, vcc
	global_load_dwordx2 v[150:151], v[10:11], off
	global_load_dwordx2 v[148:149], v[12:13], off
	global_load_dwordx2 v[146:147], v[14:15], off
	global_load_dwordx2 v[144:145], v[6:7], off
	v_add_u32_e32 v7, s0, v2
	v_lshlrev_b32_e32 v2, 3, v0
	v_lshrrev_b32_e32 v6, 3, v254
	v_and_b32_e32 v2, 56, v2
	v_mul_u32_u24_e32 v9, 0x104, v2
	v_lshlrev_b32_e32 v10, 2, v6
	v_add3_u32 v152, s0, v9, v10
	v_lshlrev_b32_e32 v10, 11, v6
	s_add_u32 s86, s10, 0x590000
	v_mul_u32_u24_e32 v5, 0x104, v5
	v_or_b32_e32 v12, 0x4000, v10
	v_or_b32_e32 v14, 0x8000, v10
	v_or_b32_e32 v16, 0xc000, v10
	v_or_b32_e32 v18, 0x10000, v10
	v_or_b32_e32 v20, 0x14000, v10
	v_or_b32_e32 v22, 0x18000, v10
	v_or_b32_e32 v24, 0x1c000, v10
	s_addc_u32 s87, s11, 0
	s_lshl_b32 s93, s91, 6
	s_lshl_b32 s88, s85, 6
	v_lshlrev_b32_e32 v4, 2, v4
	v_lshlrev_b32_e32 v6, 2, v8
	v_add_u32_e32 v153, v7, v5
	v_lshlrev_b32_e32 v2, 1, v2
	s_movk_i32 s89, 0x7fff
	s_mov_b32 s90, 0xffff0000
	v_lshlrev_b32_e32 v8, 1, v10
	v_lshlrev_b32_e32 v10, 1, v12
	v_lshlrev_b32_e32 v12, 1, v14
	v_lshlrev_b32_e32 v14, 1, v16
	v_lshlrev_b32_e32 v16, 1, v18
	v_lshlrev_b32_e32 v18, 1, v20
	v_lshlrev_b32_e32 v20, 1, v22
	v_lshlrev_b32_e32 v22, 1, v24
	s_branch .LBB0_22

.LBB0_717:
	s_cmp_lt_i32 s76, s43
	s_cselect_b32 s45, s76, s44
	s_cmp_lt_i32 s45, 0
	s_cbranch_scc1 .LBB0_741
	s_add_u32 s8, s10, 0x1cd90000
	s_addc_u32 s9, s11, 0
	s_add_u32 s46, s10, 0x3adc0000
	s_addc_u32 s47, s11, 0
	s_abs_i32 s48, s42
	v_cvt_f32_u32_e32 v1, s48
	s_sub_i32 s2, 0, s48
	s_abs_i32 s1, s45
	s_ashr_i32 s0, s45, 31
	v_rcp_iflag_f32_e32 v1, v1
	s_ashr_i32 s49, s42, 31
	s_lshr_b32 s5, s4, 6
	s_xor_b32 s0, s0, s49
	v_mul_f32_e32 v1, 0x4f7ffffe, v1
	v_cvt_u32_f32_e32 v1, v1
	v_bfe_u32 v3, v0, 2, 4
	v_lshrrev_b32_e32 v4, 3, v0
	s_movk_i32 s61, 0x81
	v_readfirstlane_b32 s50, v1
	s_mul_i32 s2, s2, s50
	s_mul_hi_u32 s2, s50, s2
	s_add_i32 s50, s50, s2
	s_mul_hi_u32 s2, s1, s50
	s_mul_i32 s3, s2, s48
	s_sub_i32 s1, s1, s3
	s_add_i32 s3, s2, 1
	s_sub_i32 s12, s1, s48
	s_cmp_ge_u32 s1, s48
	s_cselect_b32 s2, s3, s2
	s_cselect_b32 s1, s12, s1
	s_add_i32 s3, s2, 1
	s_cmp_ge_u32 s1, s48
	s_cselect_b32 s1, s3, s2
	s_xor_b32 s1, s1, s0
	s_sub_i32 s18, s1, s0
	s_mul_i32 s0, s18, s42
	s_sub_i32 s12, s45, s0
	s_lshl_b32 s0, s12, 2
	s_add_i32 s0, s0, 0
	s_add_i32 s0, s0, 0x202e0
	v_mov_b32_e32 v1, s0
	ds_read_b32 v5, v1
	v_and_or_b32 v1, v4, 48, v3
	v_or_b32_e32 v4, 64, v4
	s_movk_i32 s0, 0x70
	v_and_or_b32 v186, v4, s0, v3
	s_waitcnt lgkmcnt(0)
	v_lshlrev_b32_e32 v3, 2, v5
	v_add_u32_e32 v3, 0, v3
	v_add_u32_e32 v4, 0x20240, v3
	ds_read_b32 v4, v4
	v_add_u32_e32 v3, 0x201c0, v3
	ds_read_b32 v3, v3
	v_readfirstlane_b32 s2, v5
	s_ashr_i32 s3, s2, 31
	s_waitcnt lgkmcnt(1)
	v_sub_u32_e32 v4, s12, v4
	v_lshlrev_b32_e32 v18, 8, v4
	v_lshlrev_b32_e32 v4, 6, v5
	s_waitcnt lgkmcnt(0)
	v_add_u32_e32 v19, -1, v3
	v_add_u32_e32 v4, 0, v4
	v_or_b32_e32 v22, v18, v1
	v_add_u32_e32 v20, 0x208e0, v4
	v_min_i32_e32 v22, v22, v19
	ds_read2_b32 v[4:5], v20 offset0:1 offset1:2
	ds_read2_b32 v[6:7], v20 offset0:3 offset1:4
	ds_read2_b32 v[8:9], v20 offset0:5 offset1:6
	ds_read2_b32 v[10:11], v20 offset0:7 offset1:8
	ds_read2_b32 v[12:13], v20 offset0:9 offset1:10
	ds_read2_b32 v[14:15], v20 offset0:11 offset1:12
	ds_read2_b32 v[16:17], v20 offset0:13 offset1:14
	ds_read_b32 v21, v20 offset:60
	s_waitcnt lgkmcnt(7)
	v_cmp_ge_i32_e32 vcc, v22, v4
	v_or_b32_e32 v25, v18, v186
	v_min_i32_e32 v25, v25, v19
	v_cndmask_b32_e64 v23, 0, 1, vcc
	v_cmp_ge_i32_e32 vcc, v22, v5
	v_or_b32_e32 v28, 0x80, v18
	v_or_b32_e32 v29, v28, v1
	v_cndmask_b32_e64 v24, 0, 1, vcc
	s_waitcnt lgkmcnt(6)
	v_cmp_ge_i32_e32 vcc, v22, v6
	v_min_i32_e32 v29, v29, v19
	v_or_b32_e32 v28, v28, v186
	v_addc_co_u32_e32 v23, vcc, v23, v24, vcc
	v_cmp_ge_i32_e32 vcc, v22, v7
	v_min_i32_e32 v19, v28, v19
	s_lshl_b64 s[0:1], s[2:3], 15
	v_cndmask_b32_e64 v24, 0, 1, vcc
	s_waitcnt lgkmcnt(5)
	v_cmp_ge_i32_e32 vcc, v22, v8
	s_add_u32 s0, s46, s0
	s_addc_u32 s1, s47, s1
	v_addc_co_u32_e32 v23, vcc, v23, v24, vcc
	v_cmp_ge_i32_e32 vcc, v22, v9
	v_sub_u32_e32 v3, v3, v18
	s_nop 0
	v_cndmask_b32_e64 v24, 0, 1, vcc
	s_waitcnt lgkmcnt(4)
	v_cmp_ge_i32_e32 vcc, v22, v10
	s_nop 1
	v_addc_co_u32_e32 v23, vcc, v23, v24, vcc
	v_cmp_ge_i32_e32 vcc, v22, v11
	s_nop 1
	v_cndmask_b32_e64 v24, 0, 1, vcc
	s_waitcnt lgkmcnt(3)
	v_cmp_ge_i32_e32 vcc, v22, v12
	s_nop 1
	v_addc_co_u32_e32 v23, vcc, v23, v24, vcc
	v_cmp_ge_i32_e32 vcc, v22, v13
	s_nop 1
	v_cndmask_b32_e64 v24, 0, 1, vcc
	s_waitcnt lgkmcnt(2)
	v_cmp_ge_i32_e32 vcc, v22, v14
	s_nop 1
	v_addc_co_u32_e32 v23, vcc, v23, v24, vcc
	v_cmp_ge_i32_e32 vcc, v22, v15
	s_nop 1
	v_cndmask_b32_e64 v24, 0, 1, vcc
	s_waitcnt lgkmcnt(1)
	v_cmp_ge_i32_e32 vcc, v22, v16
	s_nop 1
	v_addc_co_u32_e32 v23, vcc, v23, v24, vcc
	v_cmp_ge_i32_e32 vcc, v22, v17
	s_nop 1
	v_cndmask_b32_e64 v24, 0, 1, vcc
	s_waitcnt lgkmcnt(0)
	v_cmp_ge_i32_e32 vcc, v22, v21
	s_nop 1
	v_addc_co_u32_e32 v23, vcc, v23, v24, vcc
	v_cmp_ge_i32_e32 vcc, v25, v4
	v_lshl_add_u32 v24, v23, 2, v20
	ds_read_b32 v24, v24
	v_cndmask_b32_e64 v26, 0, 1, vcc
	v_cmp_ge_i32_e32 vcc, v25, v5
	s_nop 1
	v_cndmask_b32_e64 v27, 0, 1, vcc
	v_cmp_ge_i32_e32 vcc, v25, v6
	s_nop 1
	v_addc_co_u32_e32 v26, vcc, v26, v27, vcc
	v_cmp_ge_i32_e32 vcc, v25, v7
	s_nop 1
	v_cndmask_b32_e64 v27, 0, 1, vcc
	v_cmp_ge_i32_e32 vcc, v25, v8
	s_nop 1
	v_addc_co_u32_e32 v26, vcc, v26, v27, vcc
	v_cmp_ge_i32_e32 vcc, v25, v9
	s_nop 1
	v_cndmask_b32_e64 v27, 0, 1, vcc
	v_cmp_ge_i32_e32 vcc, v25, v10
	s_nop 1
	v_addc_co_u32_e32 v26, vcc, v26, v27, vcc
	v_cmp_ge_i32_e32 vcc, v25, v11
	s_nop 1
	v_cndmask_b32_e64 v27, 0, 1, vcc
	v_cmp_ge_i32_e32 vcc, v25, v12
	s_nop 1
	v_addc_co_u32_e32 v26, vcc, v26, v27, vcc
	v_cmp_ge_i32_e32 vcc, v25, v13
	s_nop 1
	v_cndmask_b32_e64 v27, 0, 1, vcc
	v_cmp_ge_i32_e32 vcc, v25, v14
	s_nop 1
	v_addc_co_u32_e32 v26, vcc, v26, v27, vcc
	v_cmp_ge_i32_e32 vcc, v25, v15
	s_nop 1
	v_cndmask_b32_e64 v27, 0, 1, vcc
	v_cmp_ge_i32_e32 vcc, v25, v16
	s_nop 1
	v_addc_co_u32_e32 v26, vcc, v26, v27, vcc
	v_cmp_ge_i32_e32 vcc, v25, v17
	s_nop 1
	v_cndmask_b32_e64 v27, 0, 1, vcc
	v_cmp_ge_i32_e32 vcc, v25, v21
	s_nop 1
	v_addc_co_u32_e32 v26, vcc, v26, v27, vcc
	v_cmp_ge_i32_e32 vcc, v29, v4
	v_lshl_add_u32 v27, v26, 2, v20
	s_nop 0
	v_cndmask_b32_e64 v30, 0, 1, vcc
	v_cmp_ge_i32_e32 vcc, v29, v5
	s_nop 1
	v_cndmask_b32_e64 v31, 0, 1, vcc
	v_cmp_ge_i32_e32 vcc, v29, v6
	s_nop 1
	v_addc_co_u32_e32 v30, vcc, v30, v31, vcc
	v_cmp_ge_i32_e32 vcc, v29, v7
	s_nop 1
	v_cndmask_b32_e64 v31, 0, 1, vcc
	v_cmp_ge_i32_e32 vcc, v29, v8
	s_nop 1
	v_addc_co_u32_e32 v30, vcc, v30, v31, vcc
	v_cmp_ge_i32_e32 vcc, v29, v9
	s_nop 1
	v_cndmask_b32_e64 v31, 0, 1, vcc
	v_cmp_ge_i32_e32 vcc, v29, v10
	s_nop 1
	v_addc_co_u32_e32 v30, vcc, v30, v31, vcc
	v_cmp_ge_i32_e32 vcc, v29, v11
	s_nop 1
	v_cndmask_b32_e64 v31, 0, 1, vcc
	v_cmp_ge_i32_e32 vcc, v29, v12
	s_nop 1
	v_addc_co_u32_e32 v30, vcc, v30, v31, vcc
	v_cmp_ge_i32_e32 vcc, v29, v13
	s_nop 1
	v_cndmask_b32_e64 v31, 0, 1, vcc
	v_cmp_ge_i32_e32 vcc, v29, v14
	s_nop 1
	v_addc_co_u32_e32 v30, vcc, v30, v31, vcc
	v_cmp_ge_i32_e32 vcc, v29, v15
	s_nop 1
	v_cndmask_b32_e64 v31, 0, 1, vcc
	v_cmp_ge_i32_e32 vcc, v29, v16
	s_nop 1
	v_addc_co_u32_e32 v30, vcc, v30, v31, vcc
	v_cmp_ge_i32_e32 vcc, v29, v17
	s_nop 1
	v_cndmask_b32_e64 v31, 0, 1, vcc
	v_cmp_ge_i32_e32 vcc, v29, v21
	s_nop 1
	v_addc_co_u32_e32 v30, vcc, v30, v31, vcc
	v_cmp_ge_i32_e32 vcc, v19, v4
	v_lshl_add_u32 v31, v30, 2, v20
	s_nop 0
	v_cndmask_b32_e64 v4, 0, 1, vcc
	v_cmp_ge_i32_e32 vcc, v19, v5
	s_nop 1
	v_cndmask_b32_e64 v5, 0, 1, vcc
	v_cmp_ge_i32_e32 vcc, v19, v6
	s_nop 1
	v_addc_co_u32_e32 v4, vcc, v4, v5, vcc
	v_cmp_ge_i32_e32 vcc, v19, v7
	s_nop 1
	v_cndmask_b32_e64 v5, 0, 1, vcc
	v_cmp_ge_i32_e32 vcc, v19, v8
	s_nop 1
	v_addc_co_u32_e32 v4, vcc, v4, v5, vcc
	v_cmp_ge_i32_e32 vcc, v19, v9
	s_nop 1
	v_cndmask_b32_e64 v5, 0, 1, vcc
	v_cmp_ge_i32_e32 vcc, v19, v10
	s_nop 1
	v_addc_co_u32_e32 v4, vcc, v4, v5, vcc
	v_cmp_ge_i32_e32 vcc, v19, v11
	s_nop 1
	v_cndmask_b32_e64 v5, 0, 1, vcc
	v_cmp_ge_i32_e32 vcc, v19, v12
	s_nop 1
	v_addc_co_u32_e32 v4, vcc, v4, v5, vcc
	v_cmp_ge_i32_e32 vcc, v19, v13
	s_nop 1
	v_cndmask_b32_e64 v5, 0, 1, vcc
	v_cmp_ge_i32_e32 vcc, v19, v14
	s_nop 1
	v_addc_co_u32_e32 v4, vcc, v4, v5, vcc
	v_cmp_ge_i32_e32 vcc, v19, v15
	s_nop 1
	v_cndmask_b32_e64 v5, 0, 1, vcc
	v_cmp_ge_i32_e32 vcc, v19, v16
	s_nop 1
	v_addc_co_u32_e32 v4, vcc, v4, v5, vcc
	v_cmp_ge_i32_e32 vcc, v19, v17
	s_nop 1
	v_cndmask_b32_e64 v5, 0, 1, vcc
	v_cmp_ge_i32_e32 vcc, v19, v21
	s_nop 1
	v_addc_co_u32_e32 v8, vcc, v4, v5, vcc
	v_lshl_add_u32 v4, v8, 2, v20
	ds_read_b32 v6, v27
	ds_read_b32 v9, v31
	ds_read_b32 v10, v4
	s_waitcnt lgkmcnt(3)
	v_sub_u32_e32 v4, v22, v24
	v_lshl_add_u32 v4, v23, 9, v4
	s_waitcnt lgkmcnt(2)
	v_sub_u32_e32 v6, v25, v6
	v_ashrrev_i32_e32 v5, 31, v4
	v_lshl_add_u32 v6, v26, 9, v6
	v_lshl_add_u64 v[4:5], v[4:5], 2, s[0:1]
	v_ashrrev_i32_e32 v7, 31, v6
	v_lshl_add_u64 v[6:7], v[6:7], 2, s[0:1]
	global_load_dword v11, v[4:5], off
	global_load_dword v12, v[6:7], off
	v_lshlrev_b32_e32 v4, 4, v0
	v_and_b32_e32 v5, 32, v0
	v_bitop3_b32 v4, v4, v5, 48 bitop3:0x6c
	v_and_or_b32 v187, v0, 64, v4
	s_waitcnt lgkmcnt(1)
	v_sub_u32_e32 v4, v29, v9
	v_lshl_add_u32 v6, v8, 9, v19
	v_lshl_add_u32 v4, v30, 9, v4
	s_waitcnt lgkmcnt(0)
	v_sub_u32_e32 v6, v6, v10
	v_ashrrev_i32_e32 v5, 31, v4
	v_ashrrev_i32_e32 v7, 31, v6
	v_lshl_add_u64 v[4:5], v[4:5], 2, s[0:1]
	v_lshl_add_u64 v[6:7], v[6:7], 2, s[0:1]
	s_lshl_b32 s0, s5, 10
	global_load_dword v8, v[4:5], off
	global_load_dword v9, v[6:7], off
	s_waitcnt vmcnt(0)
	s_add_i32 s51, s0, 0
	s_waitcnt lgkmcnt(0)
	s_barrier
	s_mov_b32 m0, s51
	s_add_i32 s60, s51, 0x2000
	v_cmp_gt_i32_e64 s[0:1], s61, v3
	s_and_b64 vcc, exec, s[0:1]
	s_waitcnt vmcnt(3)
	v_lshl_or_b32 v178, v11, 12, v187
	s_waitcnt vmcnt(2)
	v_lshl_or_b32 v180, v12, 12, v187
	global_load_lds_dwordx4 v178, s[8:9]
	s_mov_b32 m0, s60
	s_waitcnt vmcnt(0)
	v_lshl_or_b32 v182, v8, 12, v187
	global_load_lds_dwordx4 v180, s[8:9]
	v_lshl_or_b32 v184, v9, 12, v187
	s_cbranch_vccnz .LBB0_720
	s_add_i32 m0, s51, 0x4000
	s_nop 0
	global_load_lds_dwordx4 v182, s[8:9]
	s_add_i32 m0, s51, 0x6000
	s_nop 0
	global_load_lds_dwordx4 v184, s[8:9]

.LBB0_721:
	s_add_i32 s0, s45, s33
	s_cmp_lt_i32 s45, s43
	s_cselect_b32 s1, s44, -1
	s_cmp_lt_i32 s0, s43
	s_cselect_b32 s45, s0, s1
	s_cmp_lt_i32 s45, 0
	s_cselect_b64 s[14:15], -1, 0
	s_and_b64 vcc, exec, s[14:15]
	v_mov_b32_e32 v209, v178
	v_mov_b32_e32 v210, v180
	v_mov_b32_e32 v211, v182
	v_mov_b32_e32 v212, v184
	s_mov_b32 s16, s18
	s_cbranch_vccnz .LBB0_723
	s_abs_i32 s1, s45
	s_mul_hi_u32 s2, s1, s50
	s_mul_i32 s3, s2, s48
	s_ashr_i32 s0, s45, 31
	s_sub_i32 s1, s1, s3
	s_xor_b32 s0, s0, s49
	s_add_i32 s3, s2, 1
	s_sub_i32 s4, s1, s48
	s_cmp_ge_u32 s1, s48
	s_cselect_b32 s2, s3, s2
	s_cselect_b32 s1, s4, s1
	s_add_i32 s3, s2, 1
	s_cmp_ge_u32 s1, s48
	s_cselect_b32 s1, s3, s2
	s_xor_b32 s1, s1, s0
	s_sub_i32 s16, s1, s0
	s_mul_i32 s0, s16, s42
	s_sub_i32 s4, s45, s0
	s_lshl_b32 s0, s4, 2
	s_add_i32 s0, s0, 0
	s_add_i32 s0, s0, 0x202e0
	v_mov_b32_e32 v30, s0
	ds_read_b32 v30, v30
	s_ashr_i32 s17, s16, 31
	s_waitcnt lgkmcnt(0)
	v_lshlrev_b32_e32 v31, 2, v30
	v_add_u32_e32 v31, 0, v31
	v_add_u32_e32 v32, 0x20240, v31
	ds_read_b32 v32, v32
	v_add_u32_e32 v31, 0x201c0, v31
	ds_read_b32 v48, v31
	v_readfirstlane_b32 s2, v30
	v_lshlrev_b32_e32 v30, 6, v30
	s_waitcnt lgkmcnt(0)
	v_sub_u32_e32 v31, s4, v32
	v_lshlrev_b32_e32 v49, 8, v31
	v_add_u32_e32 v50, -1, v48
	v_add_u32_e32 v30, 0, v30
	v_or_b32_e32 v53, v49, v1
	v_add_u32_e32 v51, 0x208e0, v30
	v_min_i32_e32 v53, v53, v50
	ds_read2_b32 v[30:31], v51 offset0:1 offset1:2
	ds_read2_b32 v[32:33], v51 offset0:3 offset1:4
	ds_read2_b32 v[38:39], v51 offset0:5 offset1:6
	ds_read2_b32 v[40:41], v51 offset0:7 offset1:8
	ds_read2_b32 v[42:43], v51 offset0:9 offset1:10
	ds_read2_b32 v[44:45], v51 offset0:11 offset1:12
	ds_read2_b32 v[46:47], v51 offset0:13 offset1:14
	ds_read_b32 v52, v51 offset:60
	s_waitcnt lgkmcnt(0)
	v_cmp_ge_i32_e32 vcc, v53, v30
	v_or_b32_e32 v56, v49, v186
	v_min_i32_e32 v56, v56, v50
	v_cndmask_b32_e64 v54, 0, 1, vcc
	v_cmp_ge_i32_e32 vcc, v53, v31
	v_or_b32_e32 v59, 0x80, v49
	v_or_b32_e32 v60, v59, v1
	v_cndmask_b32_e64 v55, 0, 1, vcc
	v_cmp_ge_i32_e32 vcc, v53, v32
	v_min_i32_e32 v60, v60, v50
	v_or_b32_e32 v59, v59, v186
	v_addc_co_u32_e32 v54, vcc, v54, v55, vcc
	v_cmp_ge_i32_e32 vcc, v53, v33
	v_min_i32_e32 v50, v59, v50
	s_ashr_i32 s3, s2, 31
	v_cndmask_b32_e64 v55, 0, 1, vcc
	v_cmp_ge_i32_e32 vcc, v53, v38
	s_lshl_b64 s[0:1], s[2:3], 23
	s_add_u32 s5, s52, s0
	v_addc_co_u32_e32 v54, vcc, v54, v55, vcc
	v_cmp_ge_i32_e32 vcc, v53, v39
	s_addc_u32 s23, s53, s1
	s_lshl_b64 s[2:3], s[2:3], 15
	v_cndmask_b32_e64 v55, 0, 1, vcc
	v_cmp_ge_i32_e32 vcc, v53, v40
	s_add_u32 s2, s46, s2
	s_addc_u32 s3, s47, s3
	v_addc_co_u32_e32 v54, vcc, v54, v55, vcc
	v_cmp_ge_i32_e32 vcc, v53, v41
	s_lshl_b32 s64, s4, 8
	s_nop 0
	v_cndmask_b32_e64 v55, 0, 1, vcc
	v_cmp_ge_i32_e32 vcc, v53, v42
	s_nop 1
	v_addc_co_u32_e32 v54, vcc, v54, v55, vcc
	v_cmp_ge_i32_e32 vcc, v53, v43
	s_nop 1
	v_cndmask_b32_e64 v55, 0, 1, vcc
	v_cmp_ge_i32_e32 vcc, v53, v44
	s_nop 1
	v_addc_co_u32_e32 v54, vcc, v54, v55, vcc
	v_cmp_ge_i32_e32 vcc, v53, v45
	s_nop 1
	v_cndmask_b32_e64 v55, 0, 1, vcc
	v_cmp_ge_i32_e32 vcc, v53, v46
	s_nop 1
	v_addc_co_u32_e32 v54, vcc, v54, v55, vcc
	v_cmp_ge_i32_e32 vcc, v53, v47
	s_nop 1
	v_cndmask_b32_e64 v55, 0, 1, vcc
	v_cmp_ge_i32_e32 vcc, v53, v52
	s_nop 1
	v_addc_co_u32_e32 v54, vcc, v54, v55, vcc
	v_cmp_ge_i32_e32 vcc, v56, v30
	v_lshl_add_u32 v55, v54, 2, v51
	ds_read_b32 v55, v55
	v_cndmask_b32_e64 v57, 0, 1, vcc
	v_cmp_ge_i32_e32 vcc, v56, v31
	s_nop 1
	v_cndmask_b32_e64 v58, 0, 1, vcc
	v_cmp_ge_i32_e32 vcc, v56, v32
	s_nop 1
	v_addc_co_u32_e32 v57, vcc, v57, v58, vcc
	v_cmp_ge_i32_e32 vcc, v56, v33
	s_nop 1
	v_cndmask_b32_e64 v58, 0, 1, vcc
	v_cmp_ge_i32_e32 vcc, v56, v38
	s_nop 1
	v_addc_co_u32_e32 v57, vcc, v57, v58, vcc
	v_cmp_ge_i32_e32 vcc, v56, v39
	s_nop 1
	v_cndmask_b32_e64 v58, 0, 1, vcc
	v_cmp_ge_i32_e32 vcc, v56, v40
	s_nop 1
	v_addc_co_u32_e32 v57, vcc, v57, v58, vcc
	v_cmp_ge_i32_e32 vcc, v56, v41
	s_nop 1
	v_cndmask_b32_e64 v58, 0, 1, vcc
	v_cmp_ge_i32_e32 vcc, v56, v42
	s_nop 1
	v_addc_co_u32_e32 v57, vcc, v57, v58, vcc
	v_cmp_ge_i32_e32 vcc, v56, v43
	s_nop 1
	v_cndmask_b32_e64 v58, 0, 1, vcc
	v_cmp_ge_i32_e32 vcc, v56, v44
	s_nop 1
	v_addc_co_u32_e32 v57, vcc, v57, v58, vcc
	v_cmp_ge_i32_e32 vcc, v56, v45
	s_nop 1
	v_cndmask_b32_e64 v58, 0, 1, vcc
	v_cmp_ge_i32_e32 vcc, v56, v46
	s_nop 1
	v_addc_co_u32_e32 v57, vcc, v57, v58, vcc
	v_cmp_ge_i32_e32 vcc, v56, v47
	s_nop 1
	v_cndmask_b32_e64 v58, 0, 1, vcc
	v_cmp_ge_i32_e32 vcc, v56, v52
	s_nop 1
	v_addc_co_u32_e32 v57, vcc, v57, v58, vcc
	v_cmp_ge_i32_e32 vcc, v60, v30
	v_lshl_add_u32 v58, v57, 2, v51
	s_nop 0
	v_cndmask_b32_e64 v61, 0, 1, vcc
	v_cmp_ge_i32_e32 vcc, v60, v31
	s_nop 1
	v_cndmask_b32_e64 v62, 0, 1, vcc
	v_cmp_ge_i32_e32 vcc, v60, v32
	s_nop 1
	v_addc_co_u32_e32 v61, vcc, v61, v62, vcc
	v_cmp_ge_i32_e32 vcc, v60, v33
	s_nop 1
	v_cndmask_b32_e64 v62, 0, 1, vcc
	v_cmp_ge_i32_e32 vcc, v60, v38
	s_nop 1
	v_addc_co_u32_e32 v61, vcc, v61, v62, vcc
	v_cmp_ge_i32_e32 vcc, v60, v39
	s_nop 1
	v_cndmask_b32_e64 v62, 0, 1, vcc
	v_cmp_ge_i32_e32 vcc, v60, v40
	s_nop 1
	v_addc_co_u32_e32 v61, vcc, v61, v62, vcc
	v_cmp_ge_i32_e32 vcc, v60, v41
	s_nop 1
	v_cndmask_b32_e64 v62, 0, 1, vcc
	v_cmp_ge_i32_e32 vcc, v60, v42
	s_nop 1
	v_addc_co_u32_e32 v61, vcc, v61, v62, vcc
	v_cmp_ge_i32_e32 vcc, v60, v43
	s_nop 1
	v_cndmask_b32_e64 v62, 0, 1, vcc
	v_cmp_ge_i32_e32 vcc, v60, v44
	s_nop 1
	v_addc_co_u32_e32 v61, vcc, v61, v62, vcc
	v_cmp_ge_i32_e32 vcc, v60, v45
	s_nop 1
	v_cndmask_b32_e64 v62, 0, 1, vcc
	v_cmp_ge_i32_e32 vcc, v60, v46
	s_nop 1
	v_addc_co_u32_e32 v61, vcc, v61, v62, vcc
	v_cmp_ge_i32_e32 vcc, v60, v47
	s_nop 1
	v_cndmask_b32_e64 v62, 0, 1, vcc
	v_cmp_ge_i32_e32 vcc, v60, v52
	s_nop 1
	v_addc_co_u32_e32 v61, vcc, v61, v62, vcc
	v_cmp_ge_i32_e32 vcc, v50, v30
	v_lshl_add_u32 v62, v61, 2, v51
	s_nop 0
	v_cndmask_b32_e64 v30, 0, 1, vcc
	v_cmp_ge_i32_e32 vcc, v50, v31
	s_nop 1
	v_cndmask_b32_e64 v31, 0, 1, vcc
	v_cmp_ge_i32_e32 vcc, v50, v32
	s_nop 1
	v_addc_co_u32_e32 v30, vcc, v30, v31, vcc
	v_cmp_ge_i32_e32 vcc, v50, v33
	s_nop 1
	v_cndmask_b32_e64 v31, 0, 1, vcc
	v_cmp_ge_i32_e32 vcc, v50, v38
	s_nop 1
	v_addc_co_u32_e32 v30, vcc, v30, v31, vcc
	v_cmp_ge_i32_e32 vcc, v50, v39
	s_nop 1
	v_cndmask_b32_e64 v31, 0, 1, vcc
	v_cmp_ge_i32_e32 vcc, v50, v40
	s_nop 1
	v_addc_co_u32_e32 v30, vcc, v30, v31, vcc
	v_cmp_ge_i32_e32 vcc, v50, v41
	s_nop 1
	v_cndmask_b32_e64 v31, 0, 1, vcc
	v_cmp_ge_i32_e32 vcc, v50, v42
	s_nop 1
	v_addc_co_u32_e32 v30, vcc, v30, v31, vcc
	v_cmp_ge_i32_e32 vcc, v50, v43
	s_nop 1
	v_cndmask_b32_e64 v31, 0, 1, vcc
	v_cmp_ge_i32_e32 vcc, v50, v44
	s_nop 1
	v_addc_co_u32_e32 v30, vcc, v30, v31, vcc
	v_cmp_ge_i32_e32 vcc, v50, v45
	s_nop 1
	v_cndmask_b32_e64 v31, 0, 1, vcc
	v_cmp_ge_i32_e32 vcc, v50, v46
	s_nop 1
	v_addc_co_u32_e32 v30, vcc, v30, v31, vcc
	v_cmp_ge_i32_e32 vcc, v50, v47
	s_nop 1
	v_cndmask_b32_e64 v31, 0, 1, vcc
	v_cmp_ge_i32_e32 vcc, v50, v52
	s_nop 1
	v_addc_co_u32_e32 v40, vcc, v30, v31, vcc
	v_lshl_add_u32 v30, v40, 2, v51
	ds_read_b32 v32, v58
	ds_read_b32 v38, v62
	ds_read_b32 v41, v30
	s_waitcnt lgkmcnt(0)
	v_sub_u32_e32 v30, v53, v55
	v_lshl_add_u32 v30, v54, 9, v30
	v_sub_u32_e32 v32, v56, v32
	v_lshl_add_u32 v32, v57, 9, v32
	v_sub_u32_e32 v38, v60, v38
	v_lshl_add_u32 v40, v40, 9, v50
	v_ashrrev_i32_e32 v31, 31, v30
	v_ashrrev_i32_e32 v33, 31, v32
	v_lshl_add_u32 v38, v61, 9, v38
	v_sub_u32_e32 v40, v40, v41
	v_lshl_add_u64 v[30:31], v[30:31], 2, s[2:3]
	v_lshl_add_u64 v[32:33], v[32:33], 2, s[2:3]
	v_ashrrev_i32_e32 v39, 31, v38
	v_ashrrev_i32_e32 v41, 31, v40
	v_lshl_add_u64 v[38:39], v[38:39], 2, s[2:3]
	v_lshl_add_u64 v[40:41], v[40:41], 2, s[2:3]
	global_load_dword v30, v[30:31], off
	s_nop 0
	global_load_dword v31, v[32:33], off
	s_nop 0
	global_load_dword v32, v[38:39], off
	global_load_dword v33, v[40:41], off
	s_add_u32 s2, s26, s0
	s_addc_u32 s3, s27, s1
	s_lshl_b64 s[0:1], s[16:17], 9
	s_add_u32 s20, s2, s0
	v_sub_u32_e32 v38, v48, v49
	s_addc_u32 s21, s3, s1
	v_cmp_gt_i32_e32 vcc, s61, v38
	s_add_u32 s22, s5, s0
	s_addc_u32 s23, s23, s1
	v_cndmask_b32_e64 v208, 0, 1, vcc
	s_waitcnt vmcnt(0)
	v_lshl_or_b32 v209, v30, 12, v187
	v_lshl_or_b32 v210, v31, 12, v187
	v_lshl_or_b32 v211, v32, 12, v187
	v_lshl_or_b32 v212, v33, 12, v187

.LBB0_849:
	s_cmp_lt_i32 s76, s53
	s_cselect_b32 s61, s76, s60
	s_cmp_lt_i32 s61, 0
	s_cbranch_scc1 .LBB0_873
	s_add_u32 s62, s10, 0x1ed90000
	s_addc_u32 s63, s11, 0
	s_abs_i32 s64, s52
	v_cvt_f32_u32_e32 v4, s64
	s_sub_i32 s2, 0, s64
	s_abs_i32 s1, s61
	s_ashr_i32 s0, s61, 31
	v_rcp_iflag_f32_e32 v4, v4
	s_ashr_i32 s65, s52, 31
	s_lshr_b32 s9, s8, 6
	s_xor_b32 s0, s0, s65
	v_mul_f32_e32 v4, 0x4f7ffffe, v4
	v_cvt_u32_f32_e32 v4, v4
	v_lshlrev_b32_e32 v1, 4, v0
	v_and_b32_e32 v2, 32, v0
	v_bfe_u32 v3, v0, 2, 4
	v_readfirstlane_b32 s66, v4
	s_mul_i32 s2, s2, s66
	s_mul_hi_u32 s2, s66, s2
	s_add_i32 s66, s66, s2
	s_mul_hi_u32 s2, s1, s66
	s_mul_i32 s3, s2, s64
	s_sub_i32 s1, s1, s3
	s_add_i32 s3, s2, 1
	s_sub_i32 s6, s1, s64
	s_cmp_ge_u32 s1, s64
	s_cselect_b32 s2, s3, s2
	s_cselect_b32 s1, s6, s1
	s_add_i32 s3, s2, 1
	s_cmp_ge_u32 s1, s64
	s_cselect_b32 s1, s3, s2
	s_xor_b32 s1, s1, s0
	s_sub_i32 s18, s1, s0
	s_mul_i32 s0, s18, s52
	s_sub_i32 s3, s61, s0
	s_lshl_b32 s0, s3, 2
	s_add_i32 s0, s0, 0
	s_add_i32 s0, s0, 0x202e0
	v_mov_b32_e32 v4, s0
	ds_read_b32 v4, v4
	v_bitop3_b32 v1, v1, v2, 48 bitop3:0x6c
	v_lshrrev_b32_e32 v2, 3, v0
	s_lshl_b32 s20, s3, 8
	v_and_or_b32 v5, v2, 48, v3
	v_or_b32_e32 v2, 64, v2
	s_movk_i32 s0, 0x70
	s_ashr_i32 s21, s20, 31
	v_and_or_b32 v2, v2, s0, v3
	s_waitcnt lgkmcnt(0)
	v_lshlrev_b32_e32 v3, 2, v4
	s_lshl_b64 s[0:1], s[20:21], 11
	v_add_u32_e32 v3, 0, v3
	s_add_u32 s22, s62, s0
	v_add_u32_e32 v6, 0x20240, v3
	v_add_u32_e32 v3, 0x201c0, v3
	s_addc_u32 s23, s63, s1
	s_lshl_b32 s0, s9, 10
	v_and_or_b32 v1, v0, 64, v1
	ds_read_b32 v6, v6
	ds_read_b32 v3, v3
	s_add_i32 s21, s0, 0
	s_waitcnt vmcnt(0)
	s_add_i32 s67, s21, 0x2000
	v_lshl_or_b32 v180, v5, 11, v1
	s_waitcnt lgkmcnt(0)
	s_barrier
	s_mov_b32 m0, s21
	v_lshl_or_b32 v182, v2, 11, v1
	global_load_lds_dwordx4 v180, s[22:23]
	s_mov_b32 m0, s67
	s_waitcnt lgkmcnt(0)
	v_subrev_u32_e32 v1, s3, v6
	global_load_lds_dwordx4 v182, s[22:23]
	v_lshlrev_b32_e32 v1, 8, v1
	v_add_u32_e32 v1, v1, v3
	s_movk_i32 s3, 0x80
	s_movk_i32 s0, 0x81
	v_cmp_lt_i32_e32 vcc, s3, v1
	v_mov_b32_e32 v187, 0
	v_readfirstlane_b32 s2, v4
	v_cmp_gt_i32_e64 s[0:1], s0, v1
	v_or_b32_e32 v184, 0x40000, v180
	v_or_b32_e32 v186, 0x40000, v182
	v_mov_b32_e32 v185, v187
	s_cbranch_vccz .LBB0_852
	s_add_i32 m0, s21, 0x4000
	v_lshl_add_u64 v[2:3], s[22:23], 0, v[186:187]
	global_load_lds_dwordx4 v184, s[22:23]
	s_add_i32 m0, s21, 0x6000
	s_nop 0
	global_load_lds_dwordx4 v[2:3], off

.LBB0_853:
	s_add_i32 s0, s61, s33
	s_cmp_lt_i32 s61, s53
	s_cselect_b32 s1, s60, -1
	s_cmp_lt_i32 s0, s53
	s_cselect_b32 s61, s0, s1
	s_cmp_lt_i32 s61, 0
	s_cselect_b64 s[24:25], -1, 0
	s_and_b64 vcc, exec, s[24:25]
	s_mov_b32 s36, s18
	s_mov_b32 s42, s20
	s_cbranch_vccnz .LBB0_855
	s_abs_i32 s1, s61
	s_mul_hi_u32 s2, s1, s66
	s_mul_i32 s3, s2, s64
	s_ashr_i32 s0, s61, 31
	s_sub_i32 s1, s1, s3
	s_xor_b32 s0, s0, s65
	s_add_i32 s3, s2, 1
	s_sub_i32 s26, s1, s64
	s_cmp_ge_u32 s1, s64
	s_cselect_b32 s2, s3, s2
	s_cselect_b32 s1, s26, s1
	s_add_i32 s3, s2, 1
	s_cmp_ge_u32 s1, s64
	s_cselect_b32 s1, s3, s2
	s_xor_b32 s1, s1, s0
	s_sub_i32 s36, s1, s0
	s_mul_i32 s0, s36, s52
	s_sub_i32 s2, s61, s0
	s_lshl_b32 s0, s2, 2
	s_add_i32 s0, s0, 0
	s_add_i32 s0, s0, 0x202e0
	v_mov_b32_e32 v1, s0
	ds_read_b32 v1, v1
	s_ashr_i32 s37, s36, 31
	s_waitcnt lgkmcnt(0)
	v_lshlrev_b32_e32 v2, 2, v1
	v_add_u32_e32 v2, 0, v2
	v_readfirstlane_b32 s0, v1
	v_add_u32_e32 v3, 0x20240, v2
	s_ashr_i32 s1, s0, 31
	ds_read_b32 v3, v3
	s_lshl_b64 s[0:1], s[0:1], 23
	v_add_u32_e32 v2, 0x201c0, v2
	s_add_u32 s3, s54, s0
	ds_read_b32 v2, v2
	s_addc_u32 s27, s55, s1
	s_lshl_b32 s42, s2, 8
	s_lshl_b64 s[0:1], s[36:37], 10
	s_add_u32 s26, s3, s0
	s_addc_u32 s27, s27, s1
	s_waitcnt lgkmcnt(0)
	v_subrev_u32_e32 v1, s2, v3
	s_add_u32 s38, s26, 0x200
	v_lshlrev_b32_e32 v1, 8, v1
	s_addc_u32 s39, s27, 0
	s_ashr_i32 s43, s42, 31
	v_add_u32_e32 v1, v1, v2
	s_lshl_b64 s[0:1], s[42:43], 11
	v_cmp_gt_i32_e32 vcc, s19, v1
	s_add_u32 s40, s62, s0
	s_addc_u32 s41, s63, s1
	v_cndmask_b32_e64 v208, 0, 1, vcc
